# code placement: FMA core of interp aligned to 64 bytes (two s_nop pads) on top of the session best
# baseline (speedup 1.0000x reference)
.Lwarm_skip:
	s_or_b64 exec, exec, s[10:11]
	v_mad_u64_u32 v[2:3], s[6:7], v71, 12, s[6:7]
	v_lshlrev_b32_e32 v4, 2, v71
	v_mov_b32_e32 v5, v69
	s_movk_i32 s6, 0xfe00
	v_lshl_add_u64 v[4:5], s[8:9], 0, v[4:5]
	v_lshl_add_u64 v[8:9], v[2:3], 0, v[6:7]
	s_mov_b32 s7, -1
	v_lshl_add_u64 v[4:5], v[4:5], 0, v[6:7]
	v_lshl_add_u64 v[2:3], v[8:9], 0, s[6:7]
	v_cmp_gt_u32_e32 vcc, 32, v1
	v_lshlrev_b32_e32 v33, 12, v10
	v_add_u32_e32 v34, v33, v6
	v_cndmask_b32_e32 v3, v3, v5, vcc
	v_cndmask_b32_e32 v2, v2, v4, vcc
	global_load_dwordx4 v[2:5], v[2:3], off
	v_and_b32_e32 v72, 1, v0
	v_lshl_add_u32 v0, v32, 4, v33
	v_lshlrev_b32_e32 v73, 4, v32
	v_lshlrev_b32_e32 v74, 6, v72
	v_xor_b32_e32 v73, v73, v74
	v_lshl_add_u32 v73, v72, 11, v73
	v_lshl_add_u32 v73, v10, 12, v73
	v_and_b32_e32 v74, 31, v1
	v_lshrrev_b32_e32 v75, 5, v1
	v_lshl_or_b32 v76, v74, 2, v71
	v_lshlrev_b32_e32 v74, 4, v74
	v_lshlrev_b32_e32 v77, 6, v75
	v_xor_b32_e32 v74, v74, v77
	v_lshl_add_u32 v74, v75, 11, v74
	v_lshl_add_u32 v74, v10, 12, v74
	v_lshlrev_b32_e32 v77, 7, v71
	v_and_b32_e32 v77, 0xe000000, v77
	v_and_b32_e32 v76, 0x3fffc, v76
	v_lshlrev_b32_e32 v75, 21, v75
	v_or3_b32 v75, v77, v75, v76
	v_lshlrev_b32_e32 v75, 2, v75
	s_mul_i32 s6, s4, 0x138800
	s_mul_hi_i32 s5, s4, 0x138800
	s_add_u32 s2, s2, s6
	s_addc_u32 s3, s3, s5
	global_load_dwordx4 v[28:31], v[8:9], off offset:512
	s_waitcnt vmcnt(1)
	ds_write_b128 v34, v[2:5]
	ds_read_b128 v[4:7], v0
	v_lshlrev_b32_e32 v0, 4, v72
	s_waitcnt lgkmcnt(0)
	v_max_i32_e32 v1, 0, v4
	v_max_i32_e32 v2, 0, v5
	v_max_i32_e32 v3, 0, v6
	v_max_i32_e32 v8, 0, v7
	v_lshl_or_b32 v35, v1, 7, v0
	v_lshl_or_b32 v36, v2, 7, v0
	v_lshl_or_b32 v37, v3, 7, v0
	v_lshl_or_b32 v38, v8, 7, v0
	global_load_dwordx4 v[20:23], v35, s[2:3]
	global_load_dwordx4 v[16:19], v35, s[2:3] offset:32
	global_load_dwordx4 v[8:11], v35, s[2:3] offset:64
	global_load_dwordx4 v[64:67], v36, s[2:3]
	global_load_dwordx4 v[60:63], v36, s[2:3] offset:32
	global_load_dwordx4 v[56:59], v36, s[2:3] offset:64
	global_load_dwordx4 v[52:55], v37, s[2:3]
	global_load_dwordx4 v[48:51], v37, s[2:3] offset:32
	global_load_dwordx4 v[44:47], v37, s[2:3] offset:64
	global_load_dwordx4 v[24:27], v38, s[2:3]
	global_load_dwordx4 v[12:15], v38, s[2:3] offset:32
	global_load_dwordx4 v[0:3], v38, s[2:3] offset:64
	s_waitcnt vmcnt(12)
	ds_write_b128 v34, v[28:31] offset:1024
	.p2alignl 6, 3212836864
	v_mul_u32_u24_e32 v28, 48, v32
	v_cmp_lt_i32_e32 vcc, -1, v4
	v_add_u32_e32 v31, v33, v28
	v_mov_b32_e32 v28, 0
	s_and_saveexec_b64 s[2:3], vcc
	ds_read_b32 v28, v31 offset:512
	s_or_b64 exec, exec, s[2:3]
	s_and_saveexec_b64 s[2:3], vcc
	ds_read_b32 v69, v31 offset:516
	s_or_b64 exec, exec, s[2:3]
	v_mov_b32_e32 v29, 0
	v_mov_b32_e32 v4, 0
	s_and_saveexec_b64 s[2:3], vcc
	ds_read_b32 v4, v31 offset:520
	s_or_b64 exec, exec, s[2:3]
	s_waitcnt vmcnt(11) lgkmcnt(0)
	v_fma_mix_f32 v30, v28, v20, v29 op_sel_hi:[0,1,0]
	v_fma_mix_f32 v20, v28, v20, v29 op_sel:[0,1,0] op_sel_hi:[0,1,0]
	v_fma_mix_f32 v32, v28, v21, v29 op_sel_hi:[0,1,0]
	v_fma_mix_f32 v21, v28, v21, v29 op_sel:[0,1,0] op_sel_hi:[0,1,0]
	v_fma_mix_f32 v33, v28, v22, v29 op_sel_hi:[0,1,0]
	v_fma_mix_f32 v22, v28, v22, v29 op_sel:[0,1,0] op_sel_hi:[0,1,0]
	v_fma_mix_f32 v34, v28, v23, v29 op_sel_hi:[0,1,0]
	v_fma_mix_f32 v23, v28, v23, v29 op_sel:[0,1,0] op_sel_hi:[0,1,0]
	s_waitcnt vmcnt(10)
	v_fma_mix_f32 v28, v69, v16, v30 op_sel_hi:[0,1,0]
	v_fma_mix_f32 v16, v69, v16, v20 op_sel:[0,1,0] op_sel_hi:[0,1,0]
	v_fma_mix_f32 v20, v69, v17, v32 op_sel_hi:[0,1,0]
	v_cmp_lt_i32_e32 vcc, -1, v5
	v_fma_mix_f32 v17, v69, v17, v21 op_sel:[0,1,0] op_sel_hi:[0,1,0]
	v_fma_mix_f32 v21, v69, v18, v33 op_sel_hi:[0,1,0]
	v_fma_mix_f32 v18, v69, v18, v22 op_sel:[0,1,0] op_sel_hi:[0,1,0]
	v_fma_mix_f32 v22, v69, v19, v34 op_sel_hi:[0,1,0]
	v_fma_mix_f32 v19, v69, v19, v23 op_sel:[0,1,0] op_sel_hi:[0,1,0]
	s_waitcnt vmcnt(9)
	v_fma_mix_f32 v40, v4, v8, v28 op_sel_hi:[0,1,0]
	v_fma_mix_f32 v36, v4, v8, v16 op_sel:[0,1,0] op_sel_hi:[0,1,0]
	v_fma_mix_f32 v32, v4, v9, v20 op_sel_hi:[0,1,0]
	v_fma_mix_f32 v28, v4, v9, v17 op_sel:[0,1,0] op_sel_hi:[0,1,0]
	v_fma_mix_f32 v20, v4, v10, v21 op_sel_hi:[0,1,0]
	v_fma_mix_f32 v16, v4, v10, v18 op_sel:[0,1,0] op_sel_hi:[0,1,0]
	v_fma_mix_f32 v8, v4, v11, v22 op_sel_hi:[0,1,0]
	v_fma_mix_f32 v4, v4, v11, v19 op_sel:[0,1,0] op_sel_hi:[0,1,0]
	s_and_saveexec_b64 s[2:3], vcc
	ds_read_b32 v29, v31 offset:524
	s_or_b64 exec, exec, s[2:3]
	v_mov_b32_e32 v5, 0
	v_mov_b32_e32 v9, 0
	s_and_saveexec_b64 s[2:3], vcc
	ds_read_b32 v9, v31 offset:528
	s_or_b64 exec, exec, s[2:3]
	s_and_saveexec_b64 s[2:3], vcc
	ds_read_b32 v5, v31 offset:532
	s_or_b64 exec, exec, s[2:3]
	v_mov_b32_e32 v10, 0
	s_waitcnt vmcnt(8) lgkmcnt(0)
	v_fma_mix_f32 v18, v29, v65, v10 op_sel_hi:[0,1,0]
	v_fma_mix_f32 v17, v29, v64, v10 op_sel:[0,1,0] op_sel_hi:[0,1,0]
	v_fma_mix_f32 v21, v29, v66, v10 op_sel_hi:[0,1,0]
	v_fma_mix_f32 v11, v29, v64, v10 op_sel_hi:[0,1,0]
	v_fma_mix_f32 v19, v29, v65, v10 op_sel:[0,1,0] op_sel_hi:[0,1,0]
	s_waitcnt vmcnt(7)
	v_fma_mix_f32 v18, v9, v61, v18 op_sel_hi:[0,1,0]
	v_fma_mix_f32 v22, v29, v66, v10 op_sel:[0,1,0] op_sel_hi:[0,1,0]
	v_fma_mix_f32 v23, v29, v67, v10 op_sel_hi:[0,1,0]
	v_fma_mix_f32 v29, v29, v67, v10 op_sel:[0,1,0] op_sel_hi:[0,1,0]
	v_fma_mix_f32 v17, v9, v60, v17 op_sel:[0,1,0] op_sel_hi:[0,1,0]
	v_fma_mix_f32 v21, v9, v62, v21 op_sel_hi:[0,1,0]
	s_waitcnt vmcnt(6)
	v_fma_mix_f32 v33, v5, v57, v18 op_sel_hi:[0,1,0]
	v_cmp_lt_i32_e32 vcc, -1, v6
	v_mov_b32_e32 v18, 0
	v_fma_mix_f32 v11, v9, v60, v11 op_sel_hi:[0,1,0]
	v_fma_mix_f32 v19, v9, v61, v19 op_sel:[0,1,0] op_sel_hi:[0,1,0]
	v_fma_mix_f32 v22, v9, v62, v22 op_sel:[0,1,0] op_sel_hi:[0,1,0]
	v_fma_mix_f32 v23, v9, v63, v23 op_sel_hi:[0,1,0]
	v_fma_mix_f32 v30, v9, v63, v29 op_sel:[0,1,0] op_sel_hi:[0,1,0]
	v_fma_mix_f32 v37, v5, v56, v17 op_sel:[0,1,0] op_sel_hi:[0,1,0]
	s_nop 0
	v_fma_mix_f32 v41, v5, v56, v11 op_sel_hi:[0,1,0]
	v_fma_mix_f32 v29, v5, v57, v19 op_sel:[0,1,0] op_sel_hi:[0,1,0]
	v_fma_mix_f32 v21, v5, v58, v21 op_sel_hi:[0,1,0]
	v_fma_mix_f32 v17, v5, v58, v22 op_sel:[0,1,0] op_sel_hi:[0,1,0]
	v_fma_mix_f32 v9, v5, v59, v23 op_sel_hi:[0,1,0]
	v_fma_mix_f32 v5, v5, v59, v30 op_sel:[0,1,0] op_sel_hi:[0,1,0]
	s_and_saveexec_b64 s[2:3], vcc
	ds_read_b32 v18, v31 offset:536
	s_or_b64 exec, exec, s[2:3]
	s_and_saveexec_b64 s[2:3], vcc
	ds_read_b32 v10, v31 offset:540
	s_or_b64 exec, exec, s[2:3]
	v_mov_b32_e32 v11, 0
	v_mov_b32_e32 v6, 0
	s_and_saveexec_b64 s[2:3], vcc
	ds_read_b32 v6, v31 offset:544
	s_or_b64 exec, exec, s[2:3]
	s_waitcnt vmcnt(5) lgkmcnt(0)
	v_fma_mix_f32 v22, v18, v52, v11 op_sel:[0,1,0] op_sel_hi:[0,1,0]
	v_fma_mix_f32 v30, v18, v53, v11 op_sel:[0,1,0] op_sel_hi:[0,1,0]
	v_fma_mix_f32 v19, v18, v52, v11 op_sel_hi:[0,1,0]
	v_fma_mix_f32 v23, v18, v53, v11 op_sel_hi:[0,1,0]
	v_fma_mix_f32 v34, v18, v54, v11 op_sel_hi:[0,1,0]
	v_fma_mix_f32 v35, v18, v54, v11 op_sel:[0,1,0] op_sel_hi:[0,1,0]
	v_fma_mix_f32 v38, v18, v55, v11 op_sel_hi:[0,1,0]
	v_fma_mix_f32 v18, v18, v55, v11 op_sel:[0,1,0] op_sel_hi:[0,1,0]
	s_waitcnt vmcnt(4)
	v_fma_mix_f32 v22, v10, v48, v22 op_sel:[0,1,0] op_sel_hi:[0,1,0]
	v_fma_mix_f32 v30, v10, v49, v30 op_sel:[0,1,0] op_sel_hi:[0,1,0]
	v_cmp_lt_i32_e32 vcc, -1, v7
	v_fma_mix_f32 v19, v10, v48, v19 op_sel_hi:[0,1,0]
	v_fma_mix_f32 v23, v10, v49, v23 op_sel_hi:[0,1,0]
	v_fma_mix_f32 v39, v10, v50, v34 op_sel_hi:[0,1,0]
	v_fma_mix_f32 v35, v10, v50, v35 op_sel:[0,1,0] op_sel_hi:[0,1,0]
	v_fma_mix_f32 v43, v10, v51, v38 op_sel_hi:[0,1,0]
	v_fma_mix_f32 v48, v10, v51, v18 op_sel:[0,1,0] op_sel_hi:[0,1,0]
	s_waitcnt vmcnt(3)
	v_fma_mix_f32 v42, v6, v44, v19 op_sel_hi:[0,1,0]
	v_fma_mix_f32 v38, v6, v44, v22 op_sel:[0,1,0] op_sel_hi:[0,1,0]
	v_fma_mix_f32 v34, v6, v45, v23 op_sel_hi:[0,1,0]
	v_fma_mix_f32 v30, v6, v45, v30 op_sel:[0,1,0] op_sel_hi:[0,1,0]
	v_fma_mix_f32 v22, v6, v46, v39 op_sel_hi:[0,1,0]
	v_fma_mix_f32 v18, v6, v46, v35 op_sel:[0,1,0] op_sel_hi:[0,1,0]
	v_fma_mix_f32 v10, v6, v47, v43 op_sel_hi:[0,1,0]
	v_fma_mix_f32 v6, v6, v47, v48 op_sel:[0,1,0] op_sel_hi:[0,1,0]
	s_and_saveexec_b64 s[2:3], vcc
	ds_read_b32 v11, v31 offset:548
	s_or_b64 exec, exec, s[2:3]
	s_load_dwordx2 s[0:1], s[0:1], 0x18
	s_ashr_i32 s5, s4, 31
	v_mov_b32_e32 v7, 0
	v_mov_b32_e32 v19, 0
	s_and_saveexec_b64 s[2:3], vcc
	ds_read_b32 v19, v31 offset:552
	s_or_b64 exec, exec, s[2:3]
	s_and_saveexec_b64 s[2:3], vcc
	ds_read_b32 v7, v31 offset:556
	s_or_b64 exec, exec, s[2:3]
	v_mov_b32_e32 v23, 0
	s_waitcnt vmcnt(2) lgkmcnt(0)
	v_fma_mix_f32 v31, v11, v24, v23 op_sel_hi:[0,1,0]
	v_fma_mix_f32 v24, v11, v24, v23 op_sel:[0,1,0] op_sel_hi:[0,1,0]
	v_fma_mix_f32 v35, v11, v25, v23 op_sel_hi:[0,1,0]
	v_fma_mix_f32 v25, v11, v25, v23 op_sel:[0,1,0] op_sel_hi:[0,1,0]
	v_fma_mix_f32 v39, v11, v26, v23 op_sel_hi:[0,1,0]
	v_fma_mix_f32 v26, v11, v26, v23 op_sel:[0,1,0] op_sel_hi:[0,1,0]
	v_fma_mix_f32 v43, v11, v27, v23 op_sel_hi:[0,1,0]
	v_fma_mix_f32 v11, v11, v27, v23 op_sel:[0,1,0] op_sel_hi:[0,1,0]
	s_waitcnt vmcnt(1)
	v_fma_mix_f32 v23, v19, v12, v31 op_sel_hi:[0,1,0]
	s_lshl_b64 s[2:3], s[4:5], 24
	v_fma_mix_f32 v12, v19, v12, v24 op_sel:[0,1,0] op_sel_hi:[0,1,0]
	v_fma_mix_f32 v24, v19, v13, v35 op_sel_hi:[0,1,0]
	v_fma_mix_f32 v13, v19, v13, v25 op_sel:[0,1,0] op_sel_hi:[0,1,0]
	v_fma_mix_f32 v25, v19, v14, v39 op_sel_hi:[0,1,0]
	v_fma_mix_f32 v14, v19, v14, v26 op_sel:[0,1,0] op_sel_hi:[0,1,0]
	v_fma_mix_f32 v26, v19, v15, v43 op_sel_hi:[0,1,0]
	v_fma_mix_f32 v15, v19, v15, v11 op_sel:[0,1,0] op_sel_hi:[0,1,0]
	s_add_u32 s0, s0, s2
	s_addc_u32 s1, s1, s3
	s_add_u32 s2, s0, 0x100000
	s_addc_u32 s3, s1, 0
	s_add_u32 s4, s0, 0x200000
	s_addc_u32 s5, s1, 0
	s_add_u32 s6, s0, 0x300000
	s_addc_u32 s7, s1, 0
	s_add_u32 s8, s0, 0x400000
	s_addc_u32 s9, s1, 0
	s_add_u32 s10, s0, 0x500000
	s_addc_u32 s11, s1, 0
	s_add_u32 s12, s0, 0x600000
	s_addc_u32 s13, s1, 0
	s_add_u32 s14, s0, 0x700000
	s_addc_u32 s15, s1, 0
	s_waitcnt vmcnt(0)
	v_fma_mix_f32 v43, v7, v0, v23 op_sel_hi:[0,1,0]
	v_fma_mix_f32 v23, v7, v2, v25 op_sel_hi:[0,1,0]
	v_fma_mix_f32 v19, v7, v2, v14 op_sel:[0,1,0] op_sel_hi:[0,1,0]
	v_fma_mix_f32 v39, v7, v0, v12 op_sel:[0,1,0] op_sel_hi:[0,1,0]
	v_fma_mix_f32 v35, v7, v1, v24 op_sel_hi:[0,1,0]
	v_fma_mix_f32 v31, v7, v1, v13 op_sel:[0,1,0] op_sel_hi:[0,1,0]
	v_fma_mix_f32 v11, v7, v3, v26 op_sel_hi:[0,1,0]
	v_fma_mix_f32 v7, v7, v3, v15 op_sel:[0,1,0] op_sel_hi:[0,1,0]
	ds_write_b128 v73, v[40:43]
	ds_write_b128 v73, v[36:39] offset:512
	ds_write_b128 v73, v[32:35] offset:1024
	ds_write_b128 v73, v[28:31] offset:1536
	ds_read_b128 v[44:47], v74
	ds_read_b128 v[48:51], v74 offset:512
	ds_read_b128 v[52:55], v74 offset:1024
	ds_read_b128 v[56:59], v74 offset:1536
	ds_write_b128 v73, v[20:23]
	ds_write_b128 v73, v[16:19] offset:512
	ds_write_b128 v73, v[8:11] offset:1024
	ds_write_b128 v73, v[4:7] offset:1536
	s_waitcnt lgkmcnt(7)
	global_store_dwordx4 v75, v[44:47], s[0:1] nt
	s_waitcnt lgkmcnt(6)
	global_store_dwordx4 v75, v[48:51], s[2:3] nt
	s_waitcnt lgkmcnt(5)
	global_store_dwordx4 v75, v[52:55], s[4:5] nt
	s_waitcnt lgkmcnt(4)
	global_store_dwordx4 v75, v[56:59], s[6:7] nt
	ds_read_b128 v[60:63], v74
	ds_read_b128 v[64:67], v74 offset:512
	ds_read_b128 v[0:3], v74 offset:1024
	ds_read_b128 v[12:15], v74 offset:1536
	s_waitcnt lgkmcnt(3)
	global_store_dwordx4 v75, v[60:63], s[8:9] nt
	s_waitcnt lgkmcnt(2)
	global_store_dwordx4 v75, v[64:67], s[10:11] nt
	s_waitcnt lgkmcnt(1)
	global_store_dwordx4 v75, v[0:3], s[12:13] nt
	s_waitcnt lgkmcnt(0)
	global_store_dwordx4 v75, v[12:15], s[14:15] nt
	s_endpgm
